# prologue de-serialisation: ATT1 unit issues its first K/V tile LDS-DMAs before the rope math instead of after the whole Q prologue
# baseline (speedup 1.0000x reference)
.LBB0_1405:
	s_cmpk_gt_i32 s68, 0x3ff
	s_cbranch_scc1 .LBB0_1353
	s_lshl_b32 s4, s68, 8
	s_ashr_i32 s0, s68, 7
	s_and_b32 s33, s4, 0x700
	s_bfe_u32 s1, s68, 0x40003
	s_add_i32 s4, s33, 0x100
	s_mul_i32 s6, s0, 0x900
	s_mul_hi_i32 s5, s0, 0x900
	s_add_u32 s62, s6, s4
	s_addc_u32 s63, s5, 0
	s_mul_i32 s4, s63, 0x1800
	s_mul_hi_u32 s5, s62, 0x1800
	s_add_i32 s5, s5, s4
	s_mul_i32 s4, s62, 0x1800
	s_add_u32 s4, s73, s4
	s_addc_u32 s5, s74, s5
	s_lshl_b32 s95, s1, 7
	s_lshl_b32 s1, s1, 8
	s_add_u32 s6, s4, s1
	s_addc_u32 s7, s5, 0
	s_mul_i32 s4, s0, 0x120000
	s_mul_hi_i32 s1, s0, 0x120000
	s_add_u32 s4, s71, s4
	s_addc_u32 s1, s72, s1
	s_lshl_b32 s5, s68, 2
	s_and_b32 s5, s5, 0x180
	s_add_u32 s64, s4, s5
	s_addc_u32 s65, s1, 0
	s_mul_hi_i32 s1, s0, 0xd80000
	s_mul_i32 s0, s0, 0xd80000
	s_add_u32 s0, s73, s0
	s_addc_u32 s1, s74, s1
	s_lshl_b32 s4, s5, 1
	v_mov_b32_e32 v187, v152
	s_add_u32 s12, s0, s4
	s_load_dwordx2 s[4:5], s[10:11], 0x88
	s_movk_i32 s0, 0xc00
	v_and_b32_e32 v188, 31, v187
	s_waitcnt vmcnt(28)
	v_or_b32_e32 v0, s82, v188
	v_mul_lo_u32 v144, v0, s0
	v_and_b32_e32 v0, 0xffffffe0, v187
	v_lshl_add_u64 v[2:3], v[144:145], 1, s[6:7]
	v_ashrrev_i32_e32 v1, 31, v0
	v_lshl_add_u64 v[6:7], v[0:1], 1, v[2:3]
	global_load_dwordx4 v[12:15], v[6:7], off offset:48
	global_load_dwordx4 v[16:19], v[6:7], off offset:32
	global_load_dwordx4 v[20:23], v[6:7], off offset:16
	global_load_dwordx4 v[2:5], v[6:7], off
	global_load_dwordx4 v[68:71], v[6:7], off offset:176
	global_load_dwordx4 v[72:75], v[6:7], off offset:160
	global_load_dwordx4 v[24:27], v[6:7], off offset:144
	global_load_dwordx4 v[28:31], v[6:7], off offset:128
	s_addc_u32 s58, s1, 0
	s_add_u32 s66, s12, 0x1400
	s_addc_u32 s67, s58, 0
	s_add_i32 s33, s33, s82
	s_lshr_b32 s0, s33, 6
	v_mov_b32_e32 v128, v145
	v_mov_b32_e32 v129, v145
	v_mov_b32_e32 v130, v145
	v_mov_b32_e32 v131, v145
	v_mov_b32_e32 v132, v145
	v_mov_b32_e32 v133, v145
	v_mov_b32_e32 v134, v145
	v_mov_b32_e32 v135, v145
	v_mov_b32_e32 v136, v145
	v_mov_b32_e32 v137, v145
	v_mov_b32_e32 v138, v145
	v_mov_b32_e32 v139, v145
	v_mov_b32_e32 v140, v145
	v_mov_b32_e32 v141, v145
	v_mov_b32_e32 v142, v145
	v_mov_b32_e32 v143, v145
	v_lshlrev_b32_e32 v190, 4, v187
	s_add_i32 s33, s84, 0
	s_add_i32 s59, s33, 0x8000
	s_mov_b32 m0, s59
	s_add_i32 s70, s33, 0x2000
	v_ashrrev_i32_e32 v189, 5, v187
	s_add_i32 s18, s33, 0xa000
	s_mov_b32 s36, 0
	s_mov_b32 s37, s36
	s_mov_b32 s38, s36
	s_mov_b32 s39, s36
	s_mov_b32 s40, s36
	s_mov_b32 s41, s36
	s_mov_b32 s42, s36
	s_mov_b32 s43, s36
	s_mov_b32 s44, s36
	s_mov_b32 s45, s36
	s_mov_b32 s46, s36
	s_mov_b32 s47, s36
	s_mov_b32 s48, s36
	s_mov_b32 s49, s36
	s_mov_b32 s50, s36
	s_mov_b32 s51, s36
	s_mov_b32 s61, 0x120000
	v_mov_b32_e32 v147, v145
	v_mov_b32_e32 v149, v145
	v_lshl_add_u32 v202, v188, 2, s81
	v_lshlrev_b32_e32 v201, 4, v189
	v_mov_b32_e32 v203, 0
	s_mov_b32 s19, 0x20000
	s_waitcnt vmcnt(7)
	v_lshlrev_b32_e32 v65, 16, v12
	s_waitcnt vmcnt(6)
	v_lshlrev_b32_e32 v64, 16, v16
	s_waitcnt vmcnt(5)
	v_lshlrev_b32_e32 v54, 16, v20
	s_waitcnt vmcnt(4)
	v_and_b32_e32 v45, 0xffff0000, v2
	v_lshlrev_b32_e32 v51, 16, v2
	v_mul_f32_e32 v36, v45, v45
	v_lshlrev_b32_e32 v40, 16, v3
	v_fmac_f32_e32 v36, v51, v51
	v_and_b32_e32 v10, 0xffff0000, v3
	v_fmac_f32_e32 v36, v40, v40
	v_lshlrev_b32_e32 v8, 16, v4
	v_fmac_f32_e32 v36, v10, v10
	v_and_b32_e32 v6, 0xffff0000, v4
	v_fmac_f32_e32 v36, v8, v8
	v_lshlrev_b32_e32 v4, 16, v5
	v_fmac_f32_e32 v36, v6, v6
	v_and_b32_e32 v2, 0xffff0000, v5
	v_fmac_f32_e32 v36, v4, v4
	v_fmac_f32_e32 v36, v2, v2
	v_and_b32_e32 v48, 0xffff0000, v20
	v_fmac_f32_e32 v36, v54, v54
	v_lshlrev_b32_e32 v42, 16, v21
	v_fmac_f32_e32 v36, v48, v48
	v_and_b32_e32 v11, 0xffff0000, v21
	v_fmac_f32_e32 v36, v42, v42
	v_lshlrev_b32_e32 v9, 16, v22
	v_fmac_f32_e32 v36, v11, v11
	v_and_b32_e32 v7, 0xffff0000, v22
	v_fmac_f32_e32 v36, v9, v9
	v_lshlrev_b32_e32 v5, 16, v23
	v_fmac_f32_e32 v36, v7, v7
	v_and_b32_e32 v3, 0xffff0000, v23
	v_fmac_f32_e32 v36, v5, v5
	v_fmac_f32_e32 v36, v3, v3
	v_and_b32_e32 v61, 0xffff0000, v16
	v_fmac_f32_e32 v36, v64, v64
	v_lshlrev_b32_e32 v58, 16, v17
	v_fmac_f32_e32 v36, v61, v61
	v_and_b32_e32 v55, 0xffff0000, v17
	v_fmac_f32_e32 v36, v58, v58
	v_lshlrev_b32_e32 v52, 16, v18
	v_fmac_f32_e32 v36, v55, v55
	v_and_b32_e32 v49, 0xffff0000, v18
	v_fmac_f32_e32 v36, v52, v52
	v_lshlrev_b32_e32 v46, 16, v19
	v_fmac_f32_e32 v36, v49, v49
	v_and_b32_e32 v43, 0xffff0000, v19
	v_fmac_f32_e32 v36, v46, v46
	v_fmac_f32_e32 v36, v43, v43
	v_and_b32_e32 v62, 0xffff0000, v12
	v_fmac_f32_e32 v36, v65, v65
	v_lshlrev_b32_e32 v59, 16, v13
	v_fmac_f32_e32 v36, v62, v62
	v_and_b32_e32 v56, 0xffff0000, v13
	v_fmac_f32_e32 v36, v59, v59
	v_lshlrev_b32_e32 v53, 16, v14
	v_fmac_f32_e32 v36, v56, v56
	v_and_b32_e32 v50, 0xffff0000, v14
	v_fmac_f32_e32 v36, v53, v53
	v_lshlrev_b32_e32 v47, 16, v15
	v_fmac_f32_e32 v36, v50, v50
	v_and_b32_e32 v44, 0xffff0000, v15
	v_fmac_f32_e32 v36, v47, v47
	v_fmac_f32_e32 v36, v44, v44
	s_waitcnt vmcnt(0)
	v_lshlrev_b32_e32 v41, 16, v28
	v_and_b32_e32 v39, 0xffff0000, v28
	v_fmac_f32_e32 v36, v41, v41
	v_lshlrev_b32_e32 v38, 16, v29
	v_fmac_f32_e32 v36, v39, v39
	v_and_b32_e32 v37, 0xffff0000, v29
	v_fmac_f32_e32 v36, v38, v38
	v_lshlrev_b32_e32 v19, 16, v30
	v_fmac_f32_e32 v36, v37, v37
	v_and_b32_e32 v18, 0xffff0000, v30
	v_fmac_f32_e32 v36, v19, v19
	v_lshlrev_b32_e32 v16, 16, v31
	v_fmac_f32_e32 v36, v18, v18
	v_and_b32_e32 v14, 0xffff0000, v31
	v_fmac_f32_e32 v36, v16, v16
	v_fmac_f32_e32 v36, v14, v14
	v_lshlrev_b32_e32 v82, 16, v24
	v_and_b32_e32 v81, 0xffff0000, v24
	v_fmac_f32_e32 v36, v82, v82
	v_lshlrev_b32_e32 v80, 16, v25
	v_fmac_f32_e32 v36, v81, v81
	v_and_b32_e32 v79, 0xffff0000, v25
	v_fmac_f32_e32 v36, v80, v80
	v_lshlrev_b32_e32 v78, 16, v26
	v_fmac_f32_e32 v36, v79, v79
	v_and_b32_e32 v67, 0xffff0000, v26
	v_fmac_f32_e32 v36, v78, v78
	v_lshlrev_b32_e32 v17, 16, v27
	v_fmac_f32_e32 v36, v67, v67
	v_and_b32_e32 v15, 0xffff0000, v27
	v_fmac_f32_e32 v36, v17, v17
	v_fmac_f32_e32 v36, v15, v15
	v_lshlrev_b32_e32 v34, 16, v72
	v_and_b32_e32 v32, 0xffff0000, v72
	v_fmac_f32_e32 v36, v34, v34
	v_lshlrev_b32_e32 v30, 16, v73
	v_fmac_f32_e32 v36, v32, v32
	v_and_b32_e32 v28, 0xffff0000, v73
	v_fmac_f32_e32 v36, v30, v30
	v_lshlrev_b32_e32 v26, 16, v74
	v_fmac_f32_e32 v36, v28, v28
	v_and_b32_e32 v24, 0xffff0000, v74
	v_fmac_f32_e32 v36, v26, v26
	v_lshlrev_b32_e32 v22, 16, v75
	v_fmac_f32_e32 v36, v24, v24
	v_and_b32_e32 v20, 0xffff0000, v75
	v_fmac_f32_e32 v36, v22, v22
	v_fmac_f32_e32 v36, v20, v20
	v_lshlrev_b32_e32 v35, 16, v68
	v_and_b32_e32 v33, 0xffff0000, v68
	v_fmac_f32_e32 v36, v35, v35
	v_lshlrev_b32_e32 v31, 16, v69
	v_fmac_f32_e32 v36, v33, v33
	v_and_b32_e32 v29, 0xffff0000, v69
	v_fmac_f32_e32 v36, v31, v31
	v_lshlrev_b32_e32 v27, 16, v70
	v_fmac_f32_e32 v36, v29, v29
	v_and_b32_e32 v25, 0xffff0000, v70
	v_fmac_f32_e32 v36, v27, v27
	v_lshlrev_b32_e32 v23, 16, v71
	v_fmac_f32_e32 v36, v25, v25
	v_and_b32_e32 v21, 0xffff0000, v71
	v_fmac_f32_e32 v36, v23, v23
	v_fmac_f32_e32 v36, v21, v21
	v_mov_b32_e32 v12, v36
	s_nop 1
	v_permlane32_swap_b32_e32 v36, v12
	v_add_f32_e32 v12, v36, v12
	v_mov_b32_e32 v13, 0x358637bd
	v_fmamk_f32 v12, v12, 0x3c000000, v13
	v_rsq_f32_e32 v36, v12
	s_waitcnt lgkmcnt(0)
	v_lshl_add_u64 v[12:13], v[0:1], 2, s[4:5]
	global_load_dwordx4 v[86:89], v[12:13], off offset:48
	global_load_dwordx4 v[90:93], v[12:13], off offset:32
	global_load_dwordx4 v[94:97], v[12:13], off offset:16
	global_load_dwordx4 v[68:71], v[12:13], off
	v_cmp_gt_u32_e64 s[4:5], 32, v187
	s_waitcnt vmcnt(0)
	v_mul_f32_e32 v0, v68, v36
	v_mul_f32_e32 v84, v0, v51
	v_mul_f32_e32 v0, v69, v36
	v_mul_f32_e32 v77, v0, v45
	v_mul_f32_e32 v0, v70, v36
	v_mul_f32_e32 v75, v0, v40
	v_mul_f32_e32 v0, v71, v36
	v_mul_f32_e32 v73, v0, v10
	v_mul_f32_e32 v0, v94, v36
	v_mul_f32_e32 v71, v0, v8
	v_mul_f32_e32 v0, v95, v36
	v_mul_f32_e32 v69, v0, v6
	v_mul_f32_e32 v0, v96, v36
	v_mul_f32_e32 v66, v0, v4
	v_mul_f32_e32 v0, v97, v36
	v_mul_f32_e32 v63, v0, v2
	v_mul_f32_e32 v0, v90, v36
	v_mul_f32_e32 v60, v0, v54
	v_mul_f32_e32 v0, v91, v36
	v_mul_f32_e32 v57, v0, v48
	v_mul_f32_e32 v0, v92, v36
	v_mul_f32_e32 v54, v0, v42
	v_mul_f32_e32 v0, v93, v36
	v_mul_f32_e32 v51, v0, v11
	v_mul_f32_e32 v0, v86, v36
	v_mul_f32_e32 v48, v0, v9
	v_mul_f32_e32 v0, v87, v36
	v_mul_f32_e32 v45, v0, v7
	v_mul_f32_e32 v0, v88, v36
	v_mul_f32_e32 v42, v0, v5
	v_mul_f32_e32 v0, v89, v36
	v_mul_f32_e32 v40, v0, v3
	global_load_dwordx4 v[0:3], v[12:13], off offset:112
	global_load_dwordx4 v[4:7], v[12:13], off offset:96
	global_load_dwordx4 v[8:11], v[12:13], off offset:80
	global_load_dwordx4 v[86:89], v[12:13], off offset:64
	s_waitcnt vmcnt(3)
	v_mul_f32_e32 v0, v36, v0
	s_waitcnt vmcnt(2)
	v_mul_f32_e32 v4, v36, v4
	s_waitcnt vmcnt(1)
	v_mul_f32_e32 v8, v36, v8
	s_waitcnt vmcnt(0)
	v_mul_f32_e32 v68, v36, v86
	v_mul_f32_e32 v74, v8, v52
	v_mul_f32_e32 v8, v36, v9
	v_mul_f32_e32 v65, v4, v65
	v_mul_f32_e32 v4, v36, v5
	v_mul_f32_e32 v53, v0, v53
	v_mul_f32_e32 v0, v36, v1
	v_mul_f32_e32 v86, v68, v64
	v_mul_f32_e32 v64, v36, v87
	v_mul_f32_e32 v72, v8, v49
	v_mul_f32_e32 v8, v36, v10
	v_mul_f32_e32 v62, v4, v62
	v_mul_f32_e32 v4, v36, v6
	v_mul_f32_e32 v50, v0, v50
	v_mul_f32_e32 v0, v36, v2
	v_mul_f32_e32 v85, v64, v61
	v_mul_f32_e32 v61, v36, v88
	v_mul_f32_e32 v70, v8, v46
	v_mul_f32_e32 v8, v36, v11
	v_mul_f32_e32 v59, v4, v59
	v_mul_f32_e32 v4, v36, v7
	v_mul_f32_e32 v47, v0, v47
	v_mul_f32_e32 v0, v36, v3
	v_mul_f32_e32 v83, v61, v58
	v_mul_f32_e32 v58, v36, v89
	v_mul_f32_e32 v68, v8, v43
	v_mul_f32_e32 v56, v4, v56
	v_mul_f32_e32 v44, v0, v44
	global_load_dwordx4 v[0:3], v[12:13], off offset:304
	global_load_dwordx4 v[4:7], v[12:13], off offset:288
	global_load_dwordx4 v[8:11], v[12:13], off offset:272
	global_load_dwordx4 v[88:91], v[12:13], off offset:256
	v_mul_f32_e32 v76, v58, v55
	s_waitcnt vmcnt(3)
	v_mul_f32_e32 v0, v36, v0
	s_waitcnt vmcnt(2)
	v_mul_f32_e32 v4, v36, v4
	s_waitcnt vmcnt(1)
	v_mul_f32_e32 v8, v36, v8
	s_waitcnt vmcnt(0)
	v_mul_f32_e32 v43, v36, v88
	v_mul_f32_e32 v64, v43, v41
	v_mul_f32_e32 v41, v36, v89
	v_mul_f32_e32 v61, v41, v39
	v_mul_f32_e32 v39, v36, v90
	v_mul_f32_e32 v52, v8, v19
	v_mul_f32_e32 v8, v36, v9
	v_mul_f32_e32 v41, v4, v82
	v_mul_f32_e32 v4, v36, v5
	v_mul_f32_e32 v19, v0, v78
	v_mul_f32_e32 v0, v36, v1
	v_mul_f32_e32 v58, v39, v38
	v_mul_f32_e32 v38, v36, v91
	v_mul_f32_e32 v49, v8, v18
	v_mul_f32_e32 v8, v36, v10
	v_mul_f32_e32 v39, v4, v81
	v_mul_f32_e32 v4, v36, v6
	v_mul_f32_e32 v18, v0, v67
	v_mul_f32_e32 v0, v36, v2
	v_mul_f32_e32 v55, v38, v37
	v_mul_f32_e32 v46, v8, v16
	v_mul_f32_e32 v8, v36, v11
	v_mul_f32_e32 v38, v4, v80
	v_mul_f32_e32 v4, v36, v7
	v_mul_f32_e32 v17, v0, v17
	v_mul_f32_e32 v0, v36, v3
	v_mul_f32_e32 v43, v8, v14
	v_mul_f32_e32 v37, v4, v79
	v_mul_f32_e32 v16, v0, v15
	global_load_dwordx4 v[0:3], v[12:13], off offset:368
	global_load_dwordx4 v[4:7], v[12:13], off offset:352
	global_load_dwordx4 v[8:11], v[12:13], off offset:336
	s_nop 0
	global_load_dwordx4 v[12:15], v[12:13], off offset:320
	v_cvt_f32_u32_e32 v78, s0
	s_movk_i32 s0, 0x60
	s_waitcnt vmcnt(3)
	v_mul_f32_e32 v0, v36, v0
	s_waitcnt vmcnt(2)
	v_mul_f32_e32 v4, v36, v4
	s_waitcnt vmcnt(1)
	v_mul_f32_e32 v8, v36, v8
	s_waitcnt vmcnt(0)
	v_add_u32_e32 v206, s84, v190
	v_ashrrev_i32_e32 v207, 31, v206
	v_lshrrev_b32_e32 v207, 25, v207
	v_add_u32_e32 v207, v206, v207
	v_ashrrev_i32_e32 v208, 7, v207
	v_and_b32_e32 v207, 0xffffff80, v207
	v_sub_u32_e32 v207, v206, v207
	v_ashrrev_i32_e32 v207, 4, v207
	v_lshrrev_b32_e32 v209, 1, v208
	v_ashrrev_i32_e32 v210, 8, v206
	v_bitop3_b32 v207, v209, v207, 7 bitop3:0x6c
	v_bfe_u32 v209, v187, 2, 2
	v_lshrrev_b32_e32 v215, 1, v187
	v_and_b32_e32 v214, 0xfffff0, v210
	v_lshrrev_b32_e32 v210, 1, v210
	v_and_or_b32 v209, v215, 8, v209
	v_lshlrev_b32_e32 v212, 3, v187
	v_and_b32_e32 v210, 4, v210
	v_lshrrev_b32_e32 v211, 4, v206
	v_and_b32_e32 v213, 24, v212
	v_or3_b32 v210, v214, v210, v209
	v_and_b32_e32 v211, 0x60, v211
	v_or_b32_e32 v211, v211, v213
	v_mul_i32_i24_e32 v210, 0xc00, v210
	v_add_u32_e32 v206, 0x2000, v206
	v_or_b32_e32 v210, v210, v211
	v_ashrrev_i32_e32 v206, 8, v206
	v_lshlrev_b32_e32 v146, 1, v210
	v_and_b32_e32 v210, 0xfffff0, v206
	v_lshrrev_b32_e32 v206, 1, v206
	v_cmp_gt_i32_e32 vcc, 8, v207
	v_lshlrev_b32_e32 v207, 4, v207
	v_and_b32_e32 v206, 4, v206
	v_cndmask_b32_e32 v207, 0, v207, vcc
	v_or3_b32 v206, v210, v206, v209
	v_mul_i32_i24_e32 v206, 0xc00, v206
	v_lshl_add_u32 v144, v208, 9, v207
	v_or_b32_e32 v206, v206, v211
	global_load_lds_dwordx4 v144, s[64:65]
	s_mov_b32 m0, s33
	v_lshlrev_b32_e32 v148, 1, v206
	v_lshl_add_u64 v[150:151], s[64:65], 0, v[144:145]
	global_load_lds_dwordx4 v146, s[66:67]
	s_mov_b32 m0, s70
	s_nop 0
	global_load_lds_dwordx4 v148, s[66:67]
	v_add_co_u32_e32 v206, vcc, 0x8000, v150
	v_addc_co_u32_e32 v207, vcc, 0, v151, vcc
	s_mov_b32 m0, s18
	s_nop 0
	global_load_lds_dwordx4 v[206:207], off
	v_mul_f32_e32 v12, v36, v12
	v_mul_f32_e32 v67, v12, v34
	v_mul_f32_e32 v12, v36, v13
	v_mul_f32_e32 v34, v12, v32
	v_mul_f32_e32 v12, v36, v14
	v_mul_f32_e32 v32, v12, v30
	v_mul_f32_e32 v12, v36, v15
	v_mul_f32_e32 v30, v12, v28
	v_mul_f32_e32 v28, v8, v26
	v_mul_f32_e32 v8, v36, v9
	v_mul_f32_e32 v15, v4, v35
	v_mul_f32_e32 v4, v36, v5
	v_mul_f32_e32 v26, v8, v24
	v_mul_f32_e32 v8, v36, v10
	v_mul_f32_e32 v13, v4, v33
	v_mul_f32_e32 v4, v36, v6
	v_mul_f32_e32 v24, v8, v22
	v_mul_f32_e32 v8, v36, v11
	v_mul_f32_e32 v11, v4, v31
	v_mul_f32_e32 v4, v36, v7
	v_mul_f32_e32 v6, v0, v27
	v_mul_f32_e32 v0, v36, v1
	v_mul_f32_e32 v22, v8, v20
	v_mul_f32_e32 v8, v4, v29
	v_mul_f32_e32 v4, v0, v25
	v_mul_f32_e32 v0, v36, v2
	v_mul_f32_e32 v2, v0, v23
	v_mul_f32_e32 v0, v36, v3
	v_mov_b32_e32 v3, v84
	v_mov_b32_e32 v5, v84
	s_nop 1
	v_permlane32_swap_b32_e32 v3, v5
	v_cndmask_b32_e64 v3, v3, v5, s[4:5]
	v_mul_f32_e32 v5, 0.15915494, v78
	v_cos_f32_e32 v7, v5
	v_sin_f32_e32 v5, v5
	v_mul_f32_e32 v0, v0, v21
	v_or_b32_e32 v1, s83, v188
	v_cvt_f32_ubyte0_e32 v1, v1
	v_mul_f32_e32 v3, v5, v3
	v_cndmask_b32_e64 v3, v3, -v3, s[4:5]
	v_fmac_f32_e32 v3, v7, v84
	v_mov_b32_e32 v5, v77
	v_mov_b32_e32 v7, v77
	s_nop 1
	v_permlane32_swap_b32_e32 v5, v7
	v_cndmask_b32_e64 v5, v5, v7, s[4:5]
	v_mul_f32_e32 v7, v154, v78
	v_mul_f32_e32 v7, 0.15915494, v7
	v_cos_f32_e32 v9, v7
	v_sin_f32_e32 v7, v7
	s_nop 0
	v_mul_f32_e32 v5, v7, v5
	v_cndmask_b32_e64 v5, v5, -v5, s[4:5]
	v_fmac_f32_e32 v5, v9, v77
	v_mov_b32_e32 v7, v75
	v_mov_b32_e32 v9, v75
	s_nop 1
	v_permlane32_swap_b32_e32 v7, v9
	v_cndmask_b32_e64 v7, v7, v9, s[4:5]
	v_mul_f32_e32 v9, v155, v78
	v_mul_f32_e32 v9, 0.15915494, v9
	v_cos_f32_e32 v10, v9
	v_sin_f32_e32 v9, v9
	s_nop 0
	v_mul_f32_e32 v7, v9, v7
	v_cndmask_b32_e64 v7, v7, -v7, s[4:5]
	v_fmac_f32_e32 v7, v10, v75
	v_mov_b32_e32 v9, v73
	v_mov_b32_e32 v10, v73
	s_nop 1
	v_permlane32_swap_b32_e32 v9, v10
	v_cndmask_b32_e64 v9, v9, v10, s[4:5]
	v_mul_f32_e32 v10, v156, v78
	v_mul_f32_e32 v10, 0.15915494, v10
	v_cos_f32_e32 v12, v10
	v_sin_f32_e32 v10, v10
	s_nop 0
	v_mul_f32_e32 v9, v10, v9
	v_cndmask_b32_e64 v9, v9, -v9, s[4:5]
	v_fmac_f32_e32 v9, v12, v73
	v_mov_b32_e32 v10, v71
	v_mov_b32_e32 v12, v71
	s_nop 1
	v_permlane32_swap_b32_e32 v10, v12
	v_cndmask_b32_e64 v10, v10, v12, s[4:5]
	v_mul_f32_e32 v12, v157, v78
	v_mul_f32_e32 v12, 0.15915494, v12
	v_cos_f32_e32 v14, v12
	v_sin_f32_e32 v12, v12
	s_nop 0
	v_mul_f32_e32 v10, v12, v10
	v_cndmask_b32_e64 v10, v10, -v10, s[4:5]
	v_fmac_f32_e32 v10, v14, v71
	v_mov_b32_e32 v12, v69
	v_mov_b32_e32 v14, v69
	s_nop 1
	v_permlane32_swap_b32_e32 v12, v14
	v_cndmask_b32_e64 v12, v12, v14, s[4:5]
	v_mul_f32_e32 v14, v158, v78
	v_mul_f32_e32 v14, 0.15915494, v14
	v_cos_f32_e32 v20, v14
	v_sin_f32_e32 v14, v14
	s_nop 0
	v_mul_f32_e32 v12, v14, v12
	v_cndmask_b32_e64 v12, v12, -v12, s[4:5]
	v_fmac_f32_e32 v12, v20, v69
	v_mov_b32_e32 v14, v66
	v_mov_b32_e32 v20, v66
	s_nop 1
	v_permlane32_swap_b32_e32 v14, v20
	v_cndmask_b32_e64 v14, v14, v20, s[4:5]
	v_mul_f32_e32 v20, v159, v78
	v_mul_f32_e32 v20, 0.15915494, v20
	v_cos_f32_e32 v21, v20
	v_sin_f32_e32 v20, v20
	s_nop 0
	v_mul_f32_e32 v14, v20, v14
	v_cndmask_b32_e64 v14, v14, -v14, s[4:5]
	v_fmac_f32_e32 v14, v21, v66
	v_mov_b32_e32 v20, v63
	v_mov_b32_e32 v21, v63
	s_nop 1
	v_permlane32_swap_b32_e32 v20, v21
	v_cndmask_b32_e64 v20, v20, v21, s[4:5]
	v_mul_f32_e32 v21, v160, v78
	v_mul_f32_e32 v21, 0.15915494, v21
	v_cos_f32_e32 v23, v21
	v_sin_f32_e32 v21, v21
	s_nop 0
	v_mul_f32_e32 v20, v21, v20
	v_cndmask_b32_e64 v20, v20, -v20, s[4:5]
	v_fmac_f32_e32 v20, v23, v63
	v_mov_b32_e32 v21, v60
	v_mov_b32_e32 v23, v60
	s_nop 1
	v_permlane32_swap_b32_e32 v21, v23
	v_cndmask_b32_e64 v21, v21, v23, s[4:5]
	v_mul_f32_e32 v23, v161, v78
	v_mul_f32_e32 v23, 0.15915494, v23
	v_cos_f32_e32 v25, v23
	v_sin_f32_e32 v23, v23
	s_nop 0
	v_mul_f32_e32 v21, v23, v21
	v_cndmask_b32_e64 v21, v21, -v21, s[4:5]
	v_fmac_f32_e32 v21, v25, v60
	v_mov_b32_e32 v23, v57
	v_mov_b32_e32 v25, v57
	s_nop 1
	v_permlane32_swap_b32_e32 v23, v25
	v_cndmask_b32_e64 v23, v23, v25, s[4:5]
	v_mul_f32_e32 v25, v162, v78
	v_mul_f32_e32 v25, 0.15915494, v25
	v_cos_f32_e32 v27, v25
	v_sin_f32_e32 v25, v25
	s_nop 0
	v_mul_f32_e32 v23, v25, v23
	v_cndmask_b32_e64 v23, v23, -v23, s[4:5]
	v_fmac_f32_e32 v23, v27, v57
	v_mov_b32_e32 v25, v54
	v_mov_b32_e32 v27, v54
	s_nop 1
	v_permlane32_swap_b32_e32 v25, v27
	v_cndmask_b32_e64 v25, v25, v27, s[4:5]
	v_mul_f32_e32 v27, v163, v78
	v_mul_f32_e32 v27, 0.15915494, v27
	v_cos_f32_e32 v29, v27
	v_sin_f32_e32 v27, v27
	s_nop 0
	v_mul_f32_e32 v25, v27, v25
	v_cndmask_b32_e64 v25, v25, -v25, s[4:5]
	v_fmac_f32_e32 v25, v29, v54
	v_mov_b32_e32 v27, v51
	v_mov_b32_e32 v29, v51
	s_nop 1
	v_permlane32_swap_b32_e32 v27, v29
	v_cndmask_b32_e64 v27, v27, v29, s[4:5]
	v_mul_f32_e32 v29, v164, v78
	v_mul_f32_e32 v29, 0.15915494, v29
	v_cos_f32_e32 v31, v29
	v_sin_f32_e32 v29, v29
	s_nop 0
	v_mul_f32_e32 v27, v29, v27
	v_cndmask_b32_e64 v27, v27, -v27, s[4:5]
	v_fmac_f32_e32 v27, v31, v51
	v_mov_b32_e32 v29, v48
	v_mov_b32_e32 v31, v48
	s_nop 1
	v_permlane32_swap_b32_e32 v29, v31
	v_cndmask_b32_e64 v29, v29, v31, s[4:5]
	v_mul_f32_e32 v31, v165, v78
	v_mul_f32_e32 v31, 0.15915494, v31
	v_cos_f32_e32 v33, v31
	v_sin_f32_e32 v31, v31
	s_nop 0
	v_mul_f32_e32 v29, v31, v29
	v_cndmask_b32_e64 v29, v29, -v29, s[4:5]
	v_fmac_f32_e32 v29, v33, v48
	v_mov_b32_e32 v31, v45
	v_mov_b32_e32 v33, v45
	s_nop 1
	v_permlane32_swap_b32_e32 v31, v33
	v_cndmask_b32_e64 v31, v31, v33, s[4:5]
	v_mul_f32_e32 v33, v166, v78
	v_mul_f32_e32 v33, 0.15915494, v33
	v_cos_f32_e32 v35, v33
	v_sin_f32_e32 v33, v33
	s_nop 0
	v_mul_f32_e32 v31, v33, v31
	v_cndmask_b32_e64 v31, v31, -v31, s[4:5]
	v_fmac_f32_e32 v31, v35, v45
	v_mov_b32_e32 v33, v42
	v_mov_b32_e32 v35, v42
	s_nop 1
	v_permlane32_swap_b32_e32 v33, v35
	v_cndmask_b32_e64 v33, v33, v35, s[4:5]
	v_mul_f32_e32 v35, v167, v78
	v_mul_f32_e32 v35, 0.15915494, v35
	v_cos_f32_e32 v36, v35
	v_sin_f32_e32 v35, v35
	s_nop 0
	v_mul_f32_e32 v33, v35, v33
	v_cndmask_b32_e64 v33, v33, -v33, s[4:5]
	v_fmac_f32_e32 v33, v36, v42
	v_mov_b32_e32 v35, v40
	v_mov_b32_e32 v36, v40
	s_nop 1
	v_permlane32_swap_b32_e32 v35, v36
	v_cndmask_b32_e64 v35, v35, v36, s[4:5]
	v_mul_f32_e32 v36, v168, v78
	v_mul_f32_e32 v36, 0.15915494, v36
	v_cos_f32_e32 v42, v36
	v_sin_f32_e32 v36, v36
	s_nop 0
	v_mul_f32_e32 v35, v36, v35
	v_cndmask_b32_e64 v35, v35, -v35, s[4:5]
	v_fmac_f32_e32 v35, v42, v40
	v_mov_b32_e32 v36, v86
	v_mov_b32_e32 v40, v86
	s_nop 1
	v_permlane32_swap_b32_e32 v36, v40
	v_cndmask_b32_e64 v36, v36, v40, s[4:5]
	v_mul_f32_e32 v40, v169, v78
	v_mul_f32_e32 v40, 0.15915494, v40
	v_cos_f32_e32 v42, v40
	v_sin_f32_e32 v40, v40
	s_nop 0
	v_mul_f32_e32 v36, v40, v36
	v_cndmask_b32_e64 v36, v36, -v36, s[4:5]
	v_fmac_f32_e32 v36, v42, v86
	v_mov_b32_e32 v40, v85
	v_mov_b32_e32 v42, v85
	s_nop 1
	v_permlane32_swap_b32_e32 v40, v42
	v_cndmask_b32_e64 v40, v40, v42, s[4:5]
	v_mul_f32_e32 v42, v170, v78
	v_mul_f32_e32 v42, 0.15915494, v42
	v_cos_f32_e32 v45, v42
	v_sin_f32_e32 v42, v42
	s_nop 0
	v_mul_f32_e32 v40, v42, v40
	v_cndmask_b32_e64 v40, v40, -v40, s[4:5]
	v_fmac_f32_e32 v40, v45, v85
	v_mov_b32_e32 v42, v83
	v_mov_b32_e32 v45, v83
	s_nop 1
	v_permlane32_swap_b32_e32 v42, v45
	v_cndmask_b32_e64 v42, v42, v45, s[4:5]
	v_mul_f32_e32 v45, v171, v78
	v_mul_f32_e32 v45, 0.15915494, v45
	v_cos_f32_e32 v48, v45
	v_sin_f32_e32 v45, v45
	s_nop 0
	v_mul_f32_e32 v42, v45, v42
	v_cndmask_b32_e64 v42, v42, -v42, s[4:5]
	v_fmac_f32_e32 v42, v48, v83
	v_mov_b32_e32 v45, v76
	v_mov_b32_e32 v48, v76
	s_nop 1
	v_permlane32_swap_b32_e32 v45, v48
	v_cndmask_b32_e64 v45, v45, v48, s[4:5]
	v_mul_f32_e32 v48, v172, v78
	v_mul_f32_e32 v48, 0.15915494, v48
	v_cos_f32_e32 v51, v48
	v_sin_f32_e32 v48, v48
	s_nop 0
	v_mul_f32_e32 v45, v48, v45
	v_cndmask_b32_e64 v45, v45, -v45, s[4:5]
	v_fmac_f32_e32 v45, v51, v76
	v_mov_b32_e32 v48, v74
	v_mov_b32_e32 v51, v74
	s_nop 1
	v_permlane32_swap_b32_e32 v48, v51
	v_cndmask_b32_e64 v48, v48, v51, s[4:5]
	v_mul_f32_e32 v51, v173, v78
	v_mul_f32_e32 v51, 0.15915494, v51
	v_cos_f32_e32 v54, v51
	v_sin_f32_e32 v51, v51
	s_nop 0
	v_mul_f32_e32 v48, v51, v48
	v_cndmask_b32_e64 v48, v48, -v48, s[4:5]
	v_fmac_f32_e32 v48, v54, v74
	v_mov_b32_e32 v51, v72
	v_mov_b32_e32 v54, v72
	s_nop 1
	v_permlane32_swap_b32_e32 v51, v54
	v_cndmask_b32_e64 v51, v51, v54, s[4:5]
	v_mul_f32_e32 v54, v174, v78
	v_mul_f32_e32 v54, 0.15915494, v54
	v_cos_f32_e32 v57, v54
	v_sin_f32_e32 v54, v54
	s_nop 0
	v_mul_f32_e32 v51, v54, v51
	v_cndmask_b32_e64 v51, v51, -v51, s[4:5]
	v_fmac_f32_e32 v51, v57, v72
	v_mov_b32_e32 v54, v70
	v_mov_b32_e32 v57, v70
	s_nop 1
	v_permlane32_swap_b32_e32 v54, v57
	v_cndmask_b32_e64 v54, v54, v57, s[4:5]
	v_mul_f32_e32 v57, v175, v78
	v_mul_f32_e32 v57, 0.15915494, v57
	v_cos_f32_e32 v60, v57
	v_sin_f32_e32 v57, v57
	s_nop 0
	v_mul_f32_e32 v54, v57, v54
	v_cndmask_b32_e64 v54, v54, -v54, s[4:5]
	v_fmac_f32_e32 v54, v60, v70
	v_mov_b32_e32 v57, v68
	v_mov_b32_e32 v60, v68
	s_nop 1
	v_permlane32_swap_b32_e32 v57, v60
	v_cndmask_b32_e64 v57, v57, v60, s[4:5]
	v_mul_f32_e32 v60, v176, v78
	v_mul_f32_e32 v60, 0.15915494, v60
	v_cos_f32_e32 v63, v60
	v_sin_f32_e32 v60, v60
	s_nop 0
	v_mul_f32_e32 v57, v60, v57
	v_cndmask_b32_e64 v57, v57, -v57, s[4:5]
	v_fmac_f32_e32 v57, v63, v68
	v_mov_b32_e32 v60, v65
	v_mov_b32_e32 v63, v65
	s_nop 1
	v_permlane32_swap_b32_e32 v60, v63
	v_cndmask_b32_e64 v60, v60, v63, s[4:5]
	v_mul_f32_e32 v63, v177, v78
	v_mul_f32_e32 v63, 0.15915494, v63
	v_cos_f32_e32 v66, v63
	v_sin_f32_e32 v63, v63
	s_nop 0
	v_mul_f32_e32 v60, v63, v60
	v_cndmask_b32_e64 v60, v60, -v60, s[4:5]
	v_fmac_f32_e32 v60, v66, v65
	v_mov_b32_e32 v63, v62
	v_mov_b32_e32 v65, v62
	s_nop 1
	v_permlane32_swap_b32_e32 v63, v65
	v_cndmask_b32_e64 v63, v63, v65, s[4:5]
	v_mul_f32_e32 v65, v178, v78
	v_mul_f32_e32 v65, 0.15915494, v65
	v_cos_f32_e32 v66, v65
	v_sin_f32_e32 v65, v65
	s_nop 0
	v_mul_f32_e32 v63, v65, v63
	v_cndmask_b32_e64 v63, v63, -v63, s[4:5]
	v_fmac_f32_e32 v63, v66, v62
	v_mov_b32_e32 v62, v59
	v_mov_b32_e32 v65, v59
	s_nop 1
	v_permlane32_swap_b32_e32 v62, v65
	v_cndmask_b32_e64 v62, v62, v65, s[4:5]
	v_mul_f32_e32 v65, v179, v78
	v_mul_f32_e32 v65, 0.15915494, v65
	v_cos_f32_e32 v66, v65
	v_sin_f32_e32 v65, v65
	s_nop 0
	v_mul_f32_e32 v62, v65, v62
	v_cndmask_b32_e64 v62, v62, -v62, s[4:5]
	v_fmac_f32_e32 v62, v66, v59
	v_mov_b32_e32 v59, v56
	v_mov_b32_e32 v65, v56
	s_nop 1
	v_permlane32_swap_b32_e32 v59, v65
	v_cndmask_b32_e64 v59, v59, v65, s[4:5]
	v_mul_f32_e32 v65, v180, v78
	v_mul_f32_e32 v65, 0.15915494, v65
	v_cos_f32_e32 v66, v65
	v_sin_f32_e32 v65, v65
	s_nop 0
	v_mul_f32_e32 v59, v65, v59
	v_cndmask_b32_e64 v59, v59, -v59, s[4:5]
	v_fmac_f32_e32 v59, v66, v56
	v_mov_b32_e32 v56, v53
	v_mov_b32_e32 v65, v53
	s_nop 1
	v_permlane32_swap_b32_e32 v56, v65
	v_cndmask_b32_e64 v56, v56, v65, s[4:5]
	v_mul_f32_e32 v65, v181, v78
	v_mul_f32_e32 v65, 0.15915494, v65
	v_cos_f32_e32 v66, v65
	v_sin_f32_e32 v65, v65
	s_nop 0
	v_mul_f32_e32 v56, v65, v56
	v_cndmask_b32_e64 v56, v56, -v56, s[4:5]
	v_fmac_f32_e32 v56, v66, v53
	v_mov_b32_e32 v53, v50
	v_mov_b32_e32 v65, v50
	s_nop 1
	v_permlane32_swap_b32_e32 v53, v65
	v_cndmask_b32_e64 v53, v53, v65, s[4:5]
	v_mul_f32_e32 v65, v182, v78
	v_mul_f32_e32 v65, 0.15915494, v65
	v_cos_f32_e32 v66, v65
	v_sin_f32_e32 v65, v65
	s_nop 0
	v_mul_f32_e32 v53, v65, v53
	v_cndmask_b32_e64 v53, v53, -v53, s[4:5]
	v_fmac_f32_e32 v53, v66, v50
	v_mov_b32_e32 v50, v47
	v_mov_b32_e32 v65, v47
	s_nop 1
	v_permlane32_swap_b32_e32 v50, v65
	v_cndmask_b32_e64 v50, v50, v65, s[4:5]
	v_mul_f32_e32 v65, v183, v78
	v_mul_f32_e32 v65, 0.15915494, v65
	v_cos_f32_e32 v66, v65
	v_sin_f32_e32 v65, v65
	s_nop 0
	v_mul_f32_e32 v50, v65, v50
	v_cndmask_b32_e64 v50, v50, -v50, s[4:5]
	v_fmac_f32_e32 v50, v66, v47
	v_mov_b32_e32 v47, v44
	v_mov_b32_e32 v65, v44
	s_nop 1
	v_permlane32_swap_b32_e32 v47, v65
	v_cndmask_b32_e64 v47, v47, v65, s[4:5]
	v_mul_f32_e32 v65, v184, v78
	v_mul_f32_e32 v65, 0.15915494, v65
	v_cos_f32_e32 v66, v65
	v_sin_f32_e32 v65, v65
	s_nop 0
	v_mul_f32_e32 v47, v65, v47
	v_cndmask_b32_e64 v47, v47, -v47, s[4:5]
	v_fmac_f32_e32 v47, v66, v44
	v_mov_b32_e32 v44, v64
	v_mov_b32_e32 v65, v64
	s_nop 1
	v_permlane32_swap_b32_e32 v44, v65
	v_cndmask_b32_e64 v44, v44, v65, s[4:5]
	v_mul_f32_e32 v65, 0.15915494, v1
	v_cos_f32_e32 v66, v65
	v_sin_f32_e32 v65, v65
	s_nop 0
	v_mul_f32_e32 v44, v65, v44
	v_cndmask_b32_e64 v44, v44, -v44, s[4:5]
	v_fmac_f32_e32 v44, v66, v64
	v_mov_b32_e32 v64, v61
	v_mov_b32_e32 v65, v61
	s_nop 1
	v_permlane32_swap_b32_e32 v64, v65
	v_cndmask_b32_e64 v64, v64, v65, s[4:5]
	v_mul_f32_e32 v65, v154, v1
	v_mul_f32_e32 v65, 0.15915494, v65
	v_cos_f32_e32 v66, v65
	v_sin_f32_e32 v65, v65
	s_nop 0
	v_mul_f32_e32 v64, v65, v64
	v_cndmask_b32_e64 v64, v64, -v64, s[4:5]
	v_fmac_f32_e32 v64, v66, v61
	v_mov_b32_e32 v61, v58
	v_mov_b32_e32 v65, v58
	s_nop 1
	v_permlane32_swap_b32_e32 v61, v65
	v_cndmask_b32_e64 v61, v61, v65, s[4:5]
	v_mul_f32_e32 v65, v155, v1
	v_mul_f32_e32 v65, 0.15915494, v65
	v_cos_f32_e32 v66, v65
	v_sin_f32_e32 v65, v65
	s_nop 0
	v_mul_f32_e32 v61, v65, v61
	v_cndmask_b32_e64 v61, v61, -v61, s[4:5]
	v_fmac_f32_e32 v61, v66, v58
	v_mov_b32_e32 v58, v55
	v_mov_b32_e32 v65, v55
	s_nop 1
	v_permlane32_swap_b32_e32 v58, v65
	v_cndmask_b32_e64 v58, v58, v65, s[4:5]
	v_mul_f32_e32 v65, v156, v1
	v_mul_f32_e32 v65, 0.15915494, v65
	v_cos_f32_e32 v66, v65
	v_sin_f32_e32 v65, v65
	s_nop 0
	v_mul_f32_e32 v58, v65, v58
	v_cndmask_b32_e64 v58, v58, -v58, s[4:5]
	v_fmac_f32_e32 v58, v66, v55
	v_mov_b32_e32 v55, v52
	v_mov_b32_e32 v65, v52
	s_nop 1
	v_permlane32_swap_b32_e32 v55, v65
	v_cndmask_b32_e64 v55, v55, v65, s[4:5]
	v_mul_f32_e32 v65, v157, v1
	v_mul_f32_e32 v65, 0.15915494, v65
	v_cos_f32_e32 v66, v65
	v_sin_f32_e32 v65, v65
	s_nop 0
	v_mul_f32_e32 v55, v65, v55
	v_cndmask_b32_e64 v55, v55, -v55, s[4:5]
	v_fmac_f32_e32 v55, v66, v52
	v_mov_b32_e32 v52, v49
	v_mov_b32_e32 v65, v49
	s_nop 1
	v_permlane32_swap_b32_e32 v52, v65
	v_cndmask_b32_e64 v52, v52, v65, s[4:5]
	v_mul_f32_e32 v65, v158, v1
	v_mul_f32_e32 v65, 0.15915494, v65
	v_cos_f32_e32 v66, v65
	v_sin_f32_e32 v65, v65
	s_nop 0
	v_mul_f32_e32 v52, v65, v52
	v_cndmask_b32_e64 v52, v52, -v52, s[4:5]
	v_fmac_f32_e32 v52, v66, v49
	v_mov_b32_e32 v49, v46
	v_mov_b32_e32 v65, v46
	s_nop 1
	v_permlane32_swap_b32_e32 v49, v65
	v_cndmask_b32_e64 v49, v49, v65, s[4:5]
	v_mul_f32_e32 v65, v159, v1
	v_mul_f32_e32 v65, 0.15915494, v65
	v_cos_f32_e32 v66, v65
	v_sin_f32_e32 v65, v65
	s_nop 0
	v_mul_f32_e32 v49, v65, v49
	v_cndmask_b32_e64 v49, v49, -v49, s[4:5]
	v_fmac_f32_e32 v49, v66, v46
	v_mov_b32_e32 v46, v43
	v_mov_b32_e32 v65, v43
	s_nop 1
	v_permlane32_swap_b32_e32 v46, v65
	v_cndmask_b32_e64 v46, v46, v65, s[4:5]
	v_mul_f32_e32 v65, v160, v1
	v_mul_f32_e32 v65, 0.15915494, v65
	v_cos_f32_e32 v66, v65
	v_sin_f32_e32 v65, v65
	s_nop 0
	v_mul_f32_e32 v46, v65, v46
	v_cndmask_b32_e64 v46, v46, -v46, s[4:5]
	v_fmac_f32_e32 v46, v66, v43
	v_mov_b32_e32 v43, v41
	v_mov_b32_e32 v65, v41
	s_nop 1
	v_permlane32_swap_b32_e32 v43, v65
	v_cndmask_b32_e64 v43, v43, v65, s[4:5]
	v_mul_f32_e32 v65, v161, v1
	v_mul_f32_e32 v65, 0.15915494, v65
	v_cos_f32_e32 v66, v65
	v_sin_f32_e32 v65, v65
	s_nop 0
	v_mul_f32_e32 v43, v65, v43
	v_cndmask_b32_e64 v43, v43, -v43, s[4:5]
	v_fmac_f32_e32 v43, v66, v41
	v_mov_b32_e32 v41, v39
	v_mov_b32_e32 v65, v39
	s_nop 1
	v_permlane32_swap_b32_e32 v41, v65
	v_cndmask_b32_e64 v41, v41, v65, s[4:5]
	v_mul_f32_e32 v65, v162, v1
	v_mul_f32_e32 v65, 0.15915494, v65
	v_cos_f32_e32 v66, v65
	v_sin_f32_e32 v65, v65
	s_nop 0
	v_mul_f32_e32 v41, v65, v41
	v_cndmask_b32_e64 v41, v41, -v41, s[4:5]
	v_fmac_f32_e32 v41, v66, v39
	v_mov_b32_e32 v39, v38
	v_mov_b32_e32 v65, v38
	s_nop 1
	v_permlane32_swap_b32_e32 v39, v65
	v_cndmask_b32_e64 v39, v39, v65, s[4:5]
	v_mul_f32_e32 v65, v163, v1
	v_mul_f32_e32 v65, 0.15915494, v65
	v_cos_f32_e32 v66, v65
	v_sin_f32_e32 v65, v65
	s_nop 0
	v_mul_f32_e32 v39, v65, v39
	v_cndmask_b32_e64 v39, v39, -v39, s[4:5]
	v_fmac_f32_e32 v39, v66, v38
	v_mov_b32_e32 v38, v37
	v_mov_b32_e32 v65, v37
	s_nop 1
	v_permlane32_swap_b32_e32 v38, v65
	v_cndmask_b32_e64 v38, v38, v65, s[4:5]
	v_mul_f32_e32 v65, v164, v1
	v_mul_f32_e32 v65, 0.15915494, v65
	v_cos_f32_e32 v66, v65
	v_sin_f32_e32 v65, v65
	s_nop 0
	v_mul_f32_e32 v38, v65, v38
	v_cndmask_b32_e64 v38, v38, -v38, s[4:5]
	v_fmac_f32_e32 v38, v66, v37
	v_mov_b32_e32 v37, v19
	v_mov_b32_e32 v65, v19
	s_nop 1
	v_permlane32_swap_b32_e32 v37, v65
	v_cndmask_b32_e64 v37, v37, v65, s[4:5]
	v_mul_f32_e32 v65, v165, v1
	v_mul_f32_e32 v65, 0.15915494, v65
	v_cos_f32_e32 v66, v65
	v_sin_f32_e32 v65, v65
	s_nop 0
	v_mul_f32_e32 v37, v65, v37
	v_cndmask_b32_e64 v37, v37, -v37, s[4:5]
	v_fmac_f32_e32 v37, v66, v19
	v_mov_b32_e32 v19, v18
	v_mov_b32_e32 v65, v18
	s_nop 1
	v_permlane32_swap_b32_e32 v19, v65
	v_cndmask_b32_e64 v19, v19, v65, s[4:5]
	v_mul_f32_e32 v65, v166, v1
	v_mul_f32_e32 v65, 0.15915494, v65
	v_cos_f32_e32 v66, v65
	v_sin_f32_e32 v65, v65
	s_nop 0
	v_mul_f32_e32 v19, v65, v19
	v_cndmask_b32_e64 v19, v19, -v19, s[4:5]
	v_fmac_f32_e32 v19, v66, v18
	v_mov_b32_e32 v18, v17
	v_mov_b32_e32 v65, v17
	s_nop 1
	v_permlane32_swap_b32_e32 v18, v65
	v_cndmask_b32_e64 v18, v18, v65, s[4:5]
	v_mul_f32_e32 v65, v167, v1
	v_mul_f32_e32 v65, 0.15915494, v65
	v_cos_f32_e32 v66, v65
	v_sin_f32_e32 v65, v65
	s_nop 0
	v_mul_f32_e32 v18, v65, v18
	v_cndmask_b32_e64 v18, v18, -v18, s[4:5]
	v_fmac_f32_e32 v18, v66, v17
	v_mov_b32_e32 v17, v16
	v_mov_b32_e32 v65, v16
	s_nop 1
	v_permlane32_swap_b32_e32 v17, v65
	v_cndmask_b32_e64 v17, v17, v65, s[4:5]
	v_mul_f32_e32 v65, v168, v1
	v_mul_f32_e32 v65, 0.15915494, v65
	v_cos_f32_e32 v66, v65
	v_sin_f32_e32 v65, v65
	s_nop 0
	v_mul_f32_e32 v17, v65, v17
	v_cndmask_b32_e64 v17, v17, -v17, s[4:5]
	v_fmac_f32_e32 v17, v66, v16
	v_mov_b32_e32 v16, v67
	v_mov_b32_e32 v65, v67
	s_nop 1
	v_permlane32_swap_b32_e32 v16, v65
	v_cndmask_b32_e64 v16, v16, v65, s[4:5]
	v_mul_f32_e32 v65, v169, v1
	v_mul_f32_e32 v65, 0.15915494, v65
	v_cos_f32_e32 v66, v65
	v_sin_f32_e32 v65, v65
	s_nop 0
	v_mul_f32_e32 v16, v65, v16
	v_cndmask_b32_e64 v16, v16, -v16, s[4:5]
	v_fmac_f32_e32 v16, v66, v67
	v_mov_b32_e32 v65, v34
	v_mov_b32_e32 v66, v34
	s_nop 1
	v_permlane32_swap_b32_e32 v65, v66
	v_cndmask_b32_e64 v65, v65, v66, s[4:5]
	v_mul_f32_e32 v66, v170, v1
	v_mul_f32_e32 v66, 0.15915494, v66
	v_cos_f32_e32 v67, v66
	v_sin_f32_e32 v66, v66
	s_nop 0
	v_mul_f32_e32 v65, v66, v65
	v_cndmask_b32_e64 v65, v65, -v65, s[4:5]
	v_fmac_f32_e32 v65, v67, v34
	v_mov_b32_e32 v34, v32
	v_mov_b32_e32 v66, v32
	s_nop 1
	v_permlane32_swap_b32_e32 v34, v66
	v_cndmask_b32_e64 v34, v34, v66, s[4:5]
	v_mul_f32_e32 v66, v171, v1
	v_mul_f32_e32 v66, 0.15915494, v66
	v_cos_f32_e32 v67, v66
	v_sin_f32_e32 v66, v66
	s_nop 0
	v_mul_f32_e32 v34, v66, v34
	v_cndmask_b32_e64 v34, v34, -v34, s[4:5]
	v_fmac_f32_e32 v34, v67, v32
	v_mov_b32_e32 v32, v30
	v_mov_b32_e32 v66, v30
	s_nop 1
	v_permlane32_swap_b32_e32 v32, v66
	v_cndmask_b32_e64 v32, v32, v66, s[4:5]
	v_mul_f32_e32 v66, v172, v1
	v_mul_f32_e32 v66, 0.15915494, v66
	v_cos_f32_e32 v67, v66
	v_sin_f32_e32 v66, v66
	s_nop 0
	v_mul_f32_e32 v32, v66, v32
	v_cndmask_b32_e64 v32, v32, -v32, s[4:5]
	v_fmac_f32_e32 v32, v67, v30
	v_mov_b32_e32 v30, v28
	v_mov_b32_e32 v66, v28
	s_nop 1
	v_permlane32_swap_b32_e32 v30, v66
	v_cndmask_b32_e64 v30, v30, v66, s[4:5]
	v_mul_f32_e32 v66, v173, v1
	v_mul_f32_e32 v66, 0.15915494, v66
	v_cos_f32_e32 v67, v66
	v_sin_f32_e32 v66, v66
	s_nop 0
	v_mul_f32_e32 v30, v66, v30
	v_cndmask_b32_e64 v30, v30, -v30, s[4:5]
	v_fmac_f32_e32 v30, v67, v28
	v_mov_b32_e32 v28, v26
	v_mov_b32_e32 v66, v26
	s_nop 1
	v_permlane32_swap_b32_e32 v28, v66
	v_cndmask_b32_e64 v28, v28, v66, s[4:5]
	v_mul_f32_e32 v66, v174, v1
	v_mul_f32_e32 v66, 0.15915494, v66
	v_cos_f32_e32 v67, v66
	v_sin_f32_e32 v66, v66
	s_nop 0
	v_mul_f32_e32 v28, v66, v28
	v_cndmask_b32_e64 v28, v28, -v28, s[4:5]
	v_fmac_f32_e32 v28, v67, v26
	v_mov_b32_e32 v26, v24
	v_mov_b32_e32 v66, v24
	s_nop 1
	v_permlane32_swap_b32_e32 v26, v66
	v_cndmask_b32_e64 v26, v26, v66, s[4:5]
	v_mul_f32_e32 v66, v175, v1
	v_mul_f32_e32 v66, 0.15915494, v66
	v_cos_f32_e32 v67, v66
	v_sin_f32_e32 v66, v66
	s_nop 0
	v_mul_f32_e32 v26, v66, v26
	v_cndmask_b32_e64 v26, v26, -v26, s[4:5]
	v_fmac_f32_e32 v26, v67, v24
	v_mov_b32_e32 v24, v22
	v_mov_b32_e32 v66, v22
	s_nop 1
	v_permlane32_swap_b32_e32 v24, v66
	v_cndmask_b32_e64 v24, v24, v66, s[4:5]
	v_mul_f32_e32 v66, v176, v1
	v_mul_f32_e32 v66, 0.15915494, v66
	v_cos_f32_e32 v67, v66
	v_sin_f32_e32 v66, v66
	s_nop 0
	v_mul_f32_e32 v24, v66, v24
	v_cndmask_b32_e64 v24, v24, -v24, s[4:5]
	v_fmac_f32_e32 v24, v67, v22
	v_mov_b32_e32 v22, v15
	v_mov_b32_e32 v66, v15
	s_nop 1
	v_permlane32_swap_b32_e32 v22, v66
	v_cndmask_b32_e64 v22, v22, v66, s[4:5]
	v_mul_f32_e32 v66, v177, v1
	v_mul_f32_e32 v66, 0.15915494, v66
	v_cos_f32_e32 v67, v66
	v_sin_f32_e32 v66, v66
	s_nop 0
	v_mul_f32_e32 v22, v66, v22
	v_cndmask_b32_e64 v22, v22, -v22, s[4:5]
	v_fmac_f32_e32 v22, v67, v15
	v_mov_b32_e32 v15, v13
	v_mov_b32_e32 v66, v13
	s_nop 1
	v_permlane32_swap_b32_e32 v15, v66
	v_cndmask_b32_e64 v15, v15, v66, s[4:5]
	v_mul_f32_e32 v66, v178, v1
	v_mul_f32_e32 v66, 0.15915494, v66
	v_cos_f32_e32 v67, v66
	v_sin_f32_e32 v66, v66
	s_nop 0
	v_mul_f32_e32 v15, v66, v15
	v_cndmask_b32_e64 v15, v15, -v15, s[4:5]
	v_fmac_f32_e32 v15, v67, v13
	v_mov_b32_e32 v13, v11
	v_mov_b32_e32 v66, v11
	s_nop 1
	v_permlane32_swap_b32_e32 v13, v66
	v_cndmask_b32_e64 v13, v13, v66, s[4:5]
	v_mul_f32_e32 v66, v179, v1
	v_mul_f32_e32 v66, 0.15915494, v66
	v_cos_f32_e32 v67, v66
	v_sin_f32_e32 v66, v66
	s_nop 0
	v_mul_f32_e32 v13, v66, v13
	v_cndmask_b32_e64 v13, v13, -v13, s[4:5]
	v_fmac_f32_e32 v13, v67, v11
	v_mov_b32_e32 v11, v8
	v_mov_b32_e32 v66, v8
	s_nop 1
	v_permlane32_swap_b32_e32 v11, v66
	v_cndmask_b32_e64 v11, v11, v66, s[4:5]
	v_mul_f32_e32 v66, v180, v1
	v_mul_f32_e32 v66, 0.15915494, v66
	v_cos_f32_e32 v67, v66
	v_sin_f32_e32 v66, v66
	s_nop 0
	v_mul_f32_e32 v11, v66, v11
	v_cndmask_b32_e64 v11, v11, -v11, s[4:5]
	v_fmac_f32_e32 v11, v67, v8
	v_mov_b32_e32 v8, v6
	v_mov_b32_e32 v66, v6
	s_nop 1
	v_permlane32_swap_b32_e32 v8, v66
	v_cndmask_b32_e64 v8, v8, v66, s[4:5]
	v_mul_f32_e32 v66, v181, v1
	v_mul_f32_e32 v66, 0.15915494, v66
	v_cos_f32_e32 v67, v66
	v_sin_f32_e32 v66, v66
	s_nop 0
	v_mul_f32_e32 v8, v66, v8
	v_cndmask_b32_e64 v8, v8, -v8, s[4:5]
	v_fmac_f32_e32 v8, v67, v6
	v_mov_b32_e32 v6, v4
	v_mov_b32_e32 v66, v4
	s_nop 1
	v_permlane32_swap_b32_e32 v6, v66
	v_cndmask_b32_e64 v6, v6, v66, s[4:5]
	v_mul_f32_e32 v66, v182, v1
	v_mul_f32_e32 v66, 0.15915494, v66
	v_cos_f32_e32 v67, v66
	v_sin_f32_e32 v66, v66
	s_nop 0
	v_mul_f32_e32 v6, v66, v6
	v_cndmask_b32_e64 v6, v6, -v6, s[4:5]
	v_fmac_f32_e32 v6, v67, v4
	v_mov_b32_e32 v4, v2
	v_mov_b32_e32 v66, v2
	s_nop 1
	v_permlane32_swap_b32_e32 v4, v66
	v_cndmask_b32_e64 v4, v4, v66, s[4:5]
	v_mul_f32_e32 v66, v183, v1
	v_mul_f32_e32 v66, 0.15915494, v66
	v_cos_f32_e32 v67, v66
	v_sin_f32_e32 v66, v66
	v_mul_f32_e32 v1, v184, v1
	v_mul_f32_e32 v1, 0.15915494, v1
	v_mul_f32_e32 v4, v66, v4
	v_cndmask_b32_e64 v4, v4, -v4, s[4:5]
	v_fmac_f32_e32 v4, v67, v2
	v_mov_b32_e32 v2, v0
	v_mov_b32_e32 v66, v0
	s_nop 1
	v_permlane32_swap_b32_e32 v2, v66
	v_cndmask_b32_e64 v2, v2, v66, s[4:5]
	v_cos_f32_e32 v66, v1
	v_sin_f32_e32 v1, v1
	s_nop 0
	v_mul_f32_e32 v1, v1, v2
	v_cndmask_b32_e64 v1, v1, -v1, s[4:5]
	v_fmac_f32_e32 v1, v66, v0
	v_med3_f32 v0, v3, s97, v185
	v_med3_f32 v2, v5, s97, v185
	v_cvt_pk_fp8_f32 v128, v0, v2
	v_med3_f32 v0, v10, s97, v185
	v_med3_f32 v2, v12, s97, v185
	v_cvt_pk_fp8_f32 v129, v0, v2
	v_med3_f32 v0, v21, s97, v185
	v_med3_f32 v2, v23, s97, v185
	v_cvt_pk_fp8_f32 v130, v0, v2
	v_med3_f32 v0, v29, s97, v185
	v_med3_f32 v2, v31, s97, v185
	v_med3_f32 v3, v7, s97, v185
	v_med3_f32 v5, v9, s97, v185
	v_cvt_pk_fp8_f32 v131, v0, v2
	v_med3_f32 v0, v36, s97, v185
	v_med3_f32 v2, v40, s97, v185
	v_cvt_pk_fp8_f32 v128, v3, v5 op_sel:[0,0,1]
	v_med3_f32 v3, v14, s97, v185
	v_med3_f32 v5, v20, s97, v185
	v_cvt_pk_fp8_f32 v132, v0, v2
	v_med3_f32 v0, v48, s97, v185
	v_med3_f32 v2, v51, s97, v185
	v_cvt_pk_fp8_f32 v129, v3, v5 op_sel:[0,0,1]
	v_med3_f32 v3, v25, s97, v185
	v_med3_f32 v5, v27, s97, v185
	v_cvt_pk_fp8_f32 v133, v0, v2
	v_med3_f32 v0, v60, s97, v185
	v_med3_f32 v2, v63, s97, v185
	v_cvt_pk_fp8_f32 v130, v3, v5 op_sel:[0,0,1]
	v_med3_f32 v3, v33, s97, v185
	v_med3_f32 v5, v35, s97, v185
	v_cvt_pk_fp8_f32 v134, v0, v2
	v_med3_f32 v0, v56, s97, v185
	v_med3_f32 v2, v53, s97, v185
	v_cvt_pk_fp8_f32 v131, v3, v5 op_sel:[0,0,1]
	v_med3_f32 v3, v42, s97, v185
	v_med3_f32 v5, v45, s97, v185
	v_cvt_pk_fp8_f32 v135, v0, v2
	v_med3_f32 v0, v44, s97, v185
	v_med3_f32 v2, v64, s97, v185
	v_cvt_pk_fp8_f32 v132, v3, v5 op_sel:[0,0,1]
	v_med3_f32 v3, v54, s97, v185
	v_med3_f32 v5, v57, s97, v185
	v_cvt_pk_fp8_f32 v136, v0, v2
	v_med3_f32 v0, v55, s97, v185
	v_med3_f32 v2, v52, s97, v185
	v_cvt_pk_fp8_f32 v133, v3, v5 op_sel:[0,0,1]
	v_med3_f32 v3, v62, s97, v185
	v_med3_f32 v5, v59, s97, v185
	v_cvt_pk_fp8_f32 v137, v0, v2
	v_med3_f32 v0, v43, s97, v185
	v_med3_f32 v2, v41, s97, v185
	v_cvt_pk_fp8_f32 v134, v3, v5 op_sel:[0,0,1]
	v_med3_f32 v3, v50, s97, v185
	v_med3_f32 v5, v47, s97, v185
	v_cvt_pk_fp8_f32 v138, v0, v2
	v_med3_f32 v0, v37, s97, v185
	v_med3_f32 v2, v19, s97, v185
	v_cvt_pk_fp8_f32 v135, v3, v5 op_sel:[0,0,1]
	v_med3_f32 v3, v61, s97, v185
	v_med3_f32 v5, v58, s97, v185
	v_cvt_pk_fp8_f32 v139, v0, v2
	v_med3_f32 v0, v16, s97, v185
	v_med3_f32 v2, v65, s97, v185
	v_cvt_pk_fp8_f32 v136, v3, v5 op_sel:[0,0,1]
	v_med3_f32 v3, v49, s97, v185
	v_med3_f32 v5, v46, s97, v185
	v_cvt_pk_fp8_f32 v140, v0, v2
	v_med3_f32 v0, v30, s97, v185
	v_med3_f32 v2, v28, s97, v185
	v_cvt_pk_fp8_f32 v137, v3, v5 op_sel:[0,0,1]
	v_med3_f32 v3, v39, s97, v185
	v_med3_f32 v5, v38, s97, v185
	v_cvt_pk_fp8_f32 v141, v0, v2
	v_med3_f32 v0, v22, s97, v185
	v_med3_f32 v2, v15, s97, v185
	v_cvt_pk_fp8_f32 v138, v3, v5 op_sel:[0,0,1]
	v_med3_f32 v3, v18, s97, v185
	v_med3_f32 v5, v17, s97, v185
	v_cvt_pk_fp8_f32 v142, v0, v2
	v_med3_f32 v0, v8, s97, v185
	v_med3_f32 v2, v6, s97, v185
	v_cvt_pk_fp8_f32 v139, v3, v5 op_sel:[0,0,1]
	v_med3_f32 v3, v34, s97, v185
	v_med3_f32 v5, v32, s97, v185
	v_cvt_pk_fp8_f32 v143, v0, v2
	v_cvt_pk_fp8_f32 v140, v3, v5 op_sel:[0,0,1]
	v_med3_f32 v3, v26, s97, v185
	v_med3_f32 v5, v24, s97, v185
	v_cvt_pk_fp8_f32 v141, v3, v5 op_sel:[0,0,1]
	v_med3_f32 v3, v13, s97, v185
	v_med3_f32 v5, v11, s97, v185
	v_cvt_pk_fp8_f32 v142, v3, v5 op_sel:[0,0,1]
	v_med3_f32 v3, v4, s97, v185
	v_med3_f32 v1, v1, s97, v185
	v_add_u32_e32 v0, s84, v190
	v_cvt_pk_fp8_f32 v143, v3, v1 op_sel:[0,0,1]
	v_ashrrev_i32_e32 v1, 31, v0
	v_lshrrev_b32_e32 v1, 25, v1
	v_add_u32_e32 v1, v0, v1
	v_ashrrev_i32_e32 v2, 7, v1
	v_and_b32_e32 v1, 0xffffff80, v1
	v_sub_u32_e32 v1, v0, v1
	v_ashrrev_i32_e32 v1, 4, v1
	v_lshrrev_b32_e32 v3, 1, v2
	v_ashrrev_i32_e32 v4, 8, v0
	v_bitop3_b32 v1, v3, v1, 7 bitop3:0x6c
	v_bfe_u32 v3, v187, 2, 2
	v_lshrrev_b32_e32 v48, 1, v187
	v_and_b32_e32 v8, 0xfffff0, v4
	v_lshrrev_b32_e32 v4, 1, v4
	v_and_or_b32 v3, v48, 8, v3
	v_lshlrev_b32_e32 v6, 3, v187
	v_and_b32_e32 v4, 4, v4
	v_lshrrev_b32_e32 v5, 4, v0
	v_and_b32_e32 v7, 24, v6
	v_or3_b32 v4, v8, v4, v3
	v_and_or_b32 v5, v5, s0, v7
	v_mul_i32_i24_e32 v4, 0xc00, v4
	v_add_u32_e32 v0, 0x2000, v0
	v_or_b32_e32 v4, v4, v5
	v_ashrrev_i32_e32 v0, 8, v0
	v_lshlrev_b32_e32 v146, 1, v4
	v_and_b32_e32 v4, 0xfffff0, v0
	v_lshrrev_b32_e32 v0, 1, v0
	v_cmp_gt_i32_e32 vcc, 8, v1
	v_lshlrev_b32_e32 v1, 4, v1
	v_and_b32_e32 v0, 4, v0
	v_cndmask_b32_e32 v1, 0, v1, vcc
	v_or3_b32 v0, v4, v0, v3
	v_mul_i32_i24_e32 v0, 0xc00, v0
	v_lshl_add_u32 v144, v2, 9, v1
	v_or_b32_e32 v0, v0, v5
	s_movk_i32 s0, 0xc0
	v_lshlrev_b32_e32 v1, 1, v187
	v_lshlrev_b32_e32 v148, 1, v0
	v_and_or_b32 v0, v190, s0, v7
	v_and_b32_e32 v1, 32, v1
	v_and_b32_e32 v2, 0x100, v6
	v_lshl_add_u64 v[150:151], s[64:65], 0, v[144:145]
	s_mov_b64 s[0:1], 0x8000
	v_or3_b32 v49, v0, v1, v2
	v_lshl_add_u64 v[0:1], v[150:151], 0, s[0:1]
	v_lshlrev_b32_e32 v50, 1, v189
	v_bitop3_b32 v0, v50, v48, 7 bitop3:0x78
	v_lshlrev_b32_e32 v51, 7, v188
	v_lshlrev_b32_e32 v0, 4, v0
	v_add_u32_e32 v1, v0, v51
	v_add_u32_e32 v191, 0, v1
	s_waitcnt vmcnt(0)
	s_waitcnt vmcnt(0) lgkmcnt(0)
	s_barrier
	ds_read_b128 v[16:19], v191 offset:32768
	v_xor_b32_e32 v1, 16, v1
	v_add_u32_e32 v192, 0, v1
	v_or_b32_e32 v52, 0x1000, v51
	ds_read_b128 v[20:23], v192 offset:32768
	ds_read_b128 v[24:27], v191 offset:36864
	v_add_u32_e32 v0, v0, v52
	v_xor_b32_e32 v0, 16, v0
	v_add_u32_e32 v193, 0, v0
	ds_read_b128 v[28:31], v193 offset:32768
	s_waitcnt lgkmcnt(2)
	v_mfma_f32_32x32x64_f8f6f4 v[32:47], v[16:23], v[128:135], 0
	v_add_u32_e32 v50, 4, v50
	v_bitop3_b32 v48, v50, v48, 7 bitop3:0x78
	v_lshlrev_b32_e32 v48, 4, v48
	v_add_u32_e32 v54, v48, v51
	v_add_u32_e32 v195, 0, v54
	v_add_u32_e32 v48, v48, v52
	ds_read_b128 v[50:53], v195 offset:32768
	v_xor_b32_e32 v54, 16, v54
	v_add_u32_e32 v196, 0, v54
	ds_read_b128 v[54:57], v196 offset:32768
	ds_read_b128 v[58:61], v195 offset:36864
	v_xor_b32_e32 v48, 16, v48
	v_add_u32_e32 v197, 0, v48
	ds_read_b128 v[62:65], v197 offset:32768
	s_mov_b64 s[0:1], 0x10000
	s_mov_b32 m0, s59
	s_waitcnt lgkmcnt(4)
	v_mfma_f32_32x32x64_f8f6f4 v[16:31], v[24:31], v[128:135], 0
	s_waitcnt lgkmcnt(0)
	s_waitcnt lgkmcnt(0)
	s_barrier
	v_mov_b64_e32 v[0:1], s[36:37]
	v_mov_b64_e32 v[14:15], s[50:51]
	v_mov_b64_e32 v[2:3], s[38:39]
	v_mov_b64_e32 v[4:5], s[40:41]
	v_mov_b64_e32 v[6:7], s[42:43]
	v_mov_b64_e32 v[8:9], s[44:45]
	v_mov_b64_e32 v[10:11], s[46:47]
	v_mov_b64_e32 v[12:13], s[48:49]
	v_mfma_f32_32x32x64_f8f6f4 v[32:47], v[50:57], v[136:143], v[32:47]
	v_mfma_f32_32x32x64_f8f6f4 v[16:31], v[58:65], v[136:143], v[16:31]
	s_nop 15
	s_nop 2
	v_max_f32_e32 v48, v33, v33
	v_max_f32_e32 v50, v32, v32
	v_max_f32_e32 v48, v50, v48
	v_max3_f32 v48, v48, v34, v35
	v_max3_f32 v48, v48, v36, v37
	v_max3_f32 v48, v48, v38, v39
	v_max3_f32 v48, v48, v40, v41
	v_max3_f32 v48, v48, v42, v43
	v_max3_f32 v48, v48, v44, v45
	v_max3_f32 v48, v48, v46, v47
	v_max3_f32 v48, v48, v16, v17
	v_max3_f32 v48, v48, v18, v19
	v_max3_f32 v48, v48, v20, v21
	v_max3_f32 v48, v48, v22, v23
	v_max3_f32 v48, v48, v24, v25
	v_max3_f32 v48, v48, v26, v27
	v_max3_f32 v48, v48, v28, v29
	v_max3_f32 v48, v48, v30, v31
	v_mov_b32_e32 v50, v48
	s_nop 1
	v_permlane32_swap_b32_e32 v48, v50
	v_max_f32_e32 v50, v50, v50
	v_max_f32_e32 v48, v48, v48
	v_max_f32_e32 v48, v48, v50
	v_add_f32_e32 v50, 0x7149f2ca, v48
	v_cmp_ge_f32_e32 vcc, s22, v50
	s_cmp_eq_u64 vcc, exec
	s_cselect_b64 vcc, -1, 0
	v_max_f32_e32 v48, 0xf149f2ca, v48
	v_cndmask_b32_e32 v198, v48, v186, vcc
	v_sub_f32_e32 v50, 0xf149f2ca, v48
	v_mul_f32_e32 v48, 0xbe0293ee, v198
	v_fmamk_f32 v32, v32, 0x3e0293ee, v48
	v_fmamk_f32 v33, v33, 0x3e0293ee, v48
	s_add_u32 s6, s12, 0x61400
	v_exp_f32_e32 v64, v32
	v_exp_f32_e32 v65, v33
	v_lshl_add_u64 v[32:33], v[150:151], 0, s[0:1]
	s_addc_u32 s7, s58, 0
	s_add_i32 s0, s33, 0x4000
	global_load_lds_dwordx4 v[32:33], off
	s_mov_b32 m0, s0
	s_add_i32 s1, s33, 0x6000
	global_load_lds_dwordx4 v146, s[6:7]
	s_mov_b32 m0, s1
	v_mul_f32_e32 v50, 0x3e0293ee, v50
	global_load_lds_dwordx4 v148, s[6:7]
	v_exp_f32_e32 v32, v50
	v_fmamk_f32 v34, v34, 0x3e0293ee, v48
	v_fmamk_f32 v35, v35, 0x3e0293ee, v48
	v_fmamk_f32 v36, v36, 0x3e0293ee, v48
	v_fmamk_f32 v37, v37, 0x3e0293ee, v48
	v_fmamk_f32 v38, v38, 0x3e0293ee, v48
	v_fmamk_f32 v39, v39, 0x3e0293ee, v48
	v_fmamk_f32 v40, v40, 0x3e0293ee, v48
	v_fmamk_f32 v41, v41, 0x3e0293ee, v48
	v_fmamk_f32 v42, v42, 0x3e0293ee, v48
	v_fmamk_f32 v43, v43, 0x3e0293ee, v48
	v_fmamk_f32 v44, v44, 0x3e0293ee, v48
	v_fmamk_f32 v45, v45, 0x3e0293ee, v48
	v_fmamk_f32 v46, v46, 0x3e0293ee, v48
	v_fmamk_f32 v47, v47, 0x3e0293ee, v48
	s_cmp_lg_u32 0, -1
	v_exp_f32_e32 v66, v34
	v_exp_f32_e32 v67, v35
	v_exp_f32_e32 v68, v36
	v_exp_f32_e32 v69, v37
	v_exp_f32_e32 v70, v38
	v_exp_f32_e32 v71, v39
	v_exp_f32_e32 v72, v40
	v_exp_f32_e32 v73, v41
	v_exp_f32_e32 v74, v42
	v_exp_f32_e32 v75, v43
	v_exp_f32_e32 v76, v44
	v_exp_f32_e32 v77, v45
	v_exp_f32_e32 v78, v46
	v_exp_f32_e32 v79, v47
	s_cselect_b32 s6, 0, 0
	v_add_u32_e32 v199, s6, v49
	s_addk_i32 s6, 0x4000
	v_cndmask_b32_e64 v200, v32, 1.0, vcc
	v_pk_fma_f32 v[94:95], v[30:31], s[54:55], v[48:49] op_sel_hi:[1,0,0]
	v_pk_fma_f32 v[92:93], v[28:29], s[54:55], v[48:49] op_sel_hi:[1,0,0]
	v_pk_fma_f32 v[90:91], v[26:27], s[54:55], v[48:49] op_sel_hi:[1,0,0]
	v_pk_fma_f32 v[88:89], v[24:25], s[54:55], v[48:49] op_sel_hi:[1,0,0]
	v_pk_fma_f32 v[86:87], v[22:23], s[54:55], v[48:49] op_sel_hi:[1,0,0]
	v_pk_fma_f32 v[84:85], v[20:21], s[54:55], v[48:49] op_sel_hi:[1,0,0]
	v_pk_fma_f32 v[82:83], v[18:19], s[54:55], v[48:49] op_sel_hi:[1,0,0]
	v_pk_fma_f32 v[80:81], v[16:17], s[54:55], v[48:49] op_sel_hi:[1,0,0]
	v_add_u32_e32 v204, s6, v49
	v_mov_b64_e32 v[62:63], v[14:15]
	v_mov_b64_e32 v[46:47], v[14:15]
	v_mov_b64_e32 v[30:31], v[14:15]
	v_mov_b64_e32 v[60:61], v[12:13]
	v_mov_b64_e32 v[58:59], v[10:11]
	v_mov_b64_e32 v[56:57], v[8:9]
	v_mov_b64_e32 v[54:55], v[6:7]
	v_mov_b64_e32 v[52:53], v[4:5]
	v_mov_b64_e32 v[50:51], v[2:3]
	v_mov_b64_e32 v[48:49], v[0:1]
	v_mov_b64_e32 v[44:45], v[12:13]
	v_mov_b64_e32 v[42:43], v[10:11]
	v_mov_b64_e32 v[40:41], v[8:9]
	v_mov_b64_e32 v[38:39], v[6:7]
	v_mov_b64_e32 v[36:37], v[4:5]
	v_mov_b64_e32 v[34:35], v[2:3]
	v_mov_b64_e32 v[32:33], v[0:1]
	v_mov_b64_e32 v[28:29], v[12:13]
	v_mov_b64_e32 v[26:27], v[10:11]
	v_mov_b64_e32 v[24:25], v[8:9]
	v_mov_b64_e32 v[22:23], v[6:7]
	v_mov_b64_e32 v[20:21], v[4:5]
	v_mov_b64_e32 v[18:19], v[2:3]
	v_mov_b64_e32 v[16:17], v[0:1]
